# MoE GEMM2 scatter: the 8 per-lane slot loads are requested from the K loop (third of four iterations) and retired by its counted waits; the epilogue no longer waits on memory before its first store (o
# baseline (speedup 1.0000x reference)
; #define LAS __attribute__((address_space(3)))
;     __device__ __forceinline__ void operator()(Acc& acc, const GUnit& u, int wr, int wc, int fr, int fq, LAS unsigned char*, int, int) const {
;         const int e = u.pm, j = u.x1 & 0xffff, n = cnt[e];
;         const int col0 = u.pn * 256 + wc * 32 + 8 * fq;
; #pragma unroll
;         for (int ai = 0; ai < 2; ++ai)
; #pragma unroll
;             for (int m = 0; m < 4; ++m) { const int idx = j * 256 + ai * HALF + wr * 64 + m * 16 + fr;
;                 if (idx < n) { const int dest = slot[(size_t)e * CAP + idx]; bf16_t* rowp = Y + (size_t)dest * 2048 + col0;
.LBB0_1429:
	s_cmp_eq_u32 s50, 2
	s_cbranch_scc0 .Lm2pf_done
	s_lshl_b32 s98, s48, 8
	s_and_b32 s98, s98, 0xffff00
	v_add_u32_e32 v134, s98, v1
	v_ashrrev_i32_e32 v135, 31, v134
	s_mov_b32 s100, s28
	s_ashr_i32 s101, s28, 31
	s_lshl_b64 s[100:101], s[100:101], 17
	s_add_u32 s98, s27, s100
	s_addc_u32 s99, s33, s101
	v_lshl_add_u64 v[252:253], v[134:135], 2, s[98:99]
	global_load_dword v244, v[252:253], off
	global_load_dword v245, v[252:253], off offset:64
	global_load_dword v246, v[252:253], off offset:128
	global_load_dword v247, v[252:253], off offset:192
	global_load_dword v248, v[252:253], off offset:512
	global_load_dword v249, v[252:253], off offset:576
	global_load_dword v250, v[252:253], off offset:640
	global_load_dword v251, v[252:253], off offset:704

; __device__ __forceinline__ unsigned cvt_pk_bf16(float lo, float hi) { const f32x2 v = {lo, hi}; return __builtin_bit_cast(unsigned, __builtin_convertvector(v, bf16x2_t)); }
;     __device__ __forceinline__ void operator()(Acc& acc, const GUnit& u, int wr, int wc, int fr, int fq, LAS unsigned char*, int, int) const {
;         const int e = u.pm, j = u.x1 & 0xffff, n = cnt[e];
;         const int col0 = u.pn * 256 + wc * 32 + 8 * fq;
; #pragma unroll
;         for (int ai = 0; ai < 2; ++ai)
; #pragma unroll
;             for (int m = 0; m < 4; ++m) { const int idx = j * 256 + ai * HALF + wr * 64 + m * 16 + fr;
;                 if (idx < n) { const int dest = slot[(size_t)e * CAP + idx]; bf16_t* rowp = Y + (size_t)dest * 2048 + col0;
; #pragma unroll
;                     for (int bj = 0; bj < 2; ++bj) { const f32x4 v0 = acc[ai][bj][m][0], v1 = acc[ai][bj][m][1];
;                         u32x4 w; w.x = cvt_pk_bf16(v0[0], v0[1]); w.y = cvt_pk_bf16(v0[2], v0[3]); w.z = cvt_pk_bf16(v1[0], v1[1]); w.w = cvt_pk_bf16(v1[2], v1[3]);
;                         *(u32x4*)(rowp + bj * HALF) = w; } } }
.LBB0_1435:
	s_lshl_b32 s6, s28, 2
	s_add_i32 s6, s6, 0
	s_add_i32 s6, s6, 0x22200
	v_mov_b32_e32 v3, s6
	ds_read_b32 v3, v3
	s_lshl_b32 s6, s48, 8
	s_and_b32 s6, s6, 0xffff00
	s_ashr_i32 s29, s28, 31
	v_lshl_or_b32 v4, s47, 8, v217
	v_add_u32_e32 v134, s6, v1
	s_lshl_b64 s[6:7], s[28:29], 17
	v_ashrrev_i32_e32 v5, 31, v4
	s_waitcnt lgkmcnt(0)
	v_cmp_lt_i32_e32 vcc, v134, v3
	v_ashrrev_i32_e32 v135, 31, v134
	s_add_u32 s30, s27, s6
	s_addc_u32 s31, s33, s7
	s_and_saveexec_b64 s[28:29], vcc
	s_cbranch_execz .LBB0_1437
	s_add_u32 s30, s27, s6
	s_addc_u32 s31, s33, s7
	v_lshl_add_u64 v[136:137], v[134:135], 2, s[30:31]
	v_mov_b32_e32 v136, v244
	v_cvt_pk_bf16_f32 v122, v122, v123
	v_cvt_pk_bf16_f32 v123, v124, v125
	v_cvt_pk_bf16_f32 v124, v118, v119
	v_cvt_pk_bf16_f32 v130, v130, v131
	v_cvt_pk_bf16_f32 v131, v132, v133
	v_cvt_pk_bf16_f32 v132, v126, v127
	v_cvt_pk_bf16_f32 v133, v128, v129
	v_cvt_pk_bf16_f32 v125, v120, v121
	v_ashrrev_i32_e32 v137, 31, v136
	v_lshlrev_b64 v[118:119], 12, v[136:137]
	v_lshl_add_u64 v[118:119], s[8:9], 0, v[118:119]
	v_lshl_add_u64 v[118:119], v[4:5], 1, v[118:119]
	global_store_dwordx4 v[118:119], v[130:133], off
	global_store_dwordx4 v[118:119], v[122:125], off offset:256
